# speedup vs baseline: 1.0417x; 1.0051x over previous
.LBB2_28:
	s_and_b32 s0, s2, 0xffffff80
	s_or_b32 s0, s3, s0
	s_or_b32 s0, s0, s24
	s_mul_hi_u32 s1, s0, 0x2300
	s_mulk_i32 s0, 0x2300
	s_waitcnt lgkmcnt(0)
	s_barrier
	s_add_u32 s0, s16, s0
	s_addc_u32 s1, s17, s1
	v_lshlrev_b32_e32 v4, 4, v0
	v_add_u32_e32 v3, 0xc800, v4
	ds_read_b128 v[6:9], v3
	ds_read_b128 v[10:13], v3 offset:8960
	v_cmp_gt_u32_e32 vcc, 48, v0
	s_waitcnt lgkmcnt(0)
	v_add_f32_e32 v6, v6, v10
	v_add_f32_e32 v7, v7, v11
	v_add_f32_e32 v8, v8, v12
	v_add_f32_e32 v9, v9, v13
	global_store_dwordx4 v4, v[6:9], s[0:1] sc1
	s_and_saveexec_b64 s[2:3], vcc
	s_cbranch_execz .Lk2_pdone
	ds_read_b128 v[6:9], v3 offset:8192
	ds_read_b128 v[10:13], v3 offset:17152
	v_add_u32_e32 v4, 0x2000, v4
	s_waitcnt lgkmcnt(0)
	v_add_f32_e32 v6, v6, v10
	v_add_f32_e32 v7, v7, v11
	v_add_f32_e32 v8, v8, v12
	v_add_f32_e32 v9, v9, v13
	global_store_dwordx4 v4, v[6:9], s[0:1] sc1
